# speedup vs baseline: 1.0416x; 1.0035x over previous
_Z11prep_kernelPKfS0_S0_S0_S0_S0_S0_S0_S0_PKiPDv8_DF16bS4_PfS5_S5_PiPt:
	s_load_dwordx4 s[16:19], s[0:1], 0x0
	s_load_dwordx4 s[20:23], s[0:1], 0x10
	s_load_dwordx4 s[24:27], s[0:1], 0x20
	s_load_dwordx4 s[28:31], s[0:1], 0x30
	s_load_dwordx4 s[32:35], s[0:1], 0x40
	s_load_dwordx2 s[36:37], s[0:1], 0x80
	s_load_dwordx4 s[60:63], s[0:1], 0x50
	s_load_dwordx4 s[64:67], s[0:1], 0x60
	s_load_dwordx4 s[68:71], s[0:1], 0x70
	v_and_b32_e32 v126, 63, v0
	v_lshrrev_b32_e32 v128, 6, v0
	v_and_b32_e32 v1, 15, v0
	v_bfe_u32 v24, v0, 4, 2
	v_lshl_or_b32 v107, v128, 4, v1
	v_lshlrev_b32_e32 v106, 2, v107
	v_lshlrev_b32_e32 v127, 2, v0
	v_lshlrev_b32_e32 v25, 1, v107
	v_and_b32_e32 v26, 48, v0
	v_mul_u32_u24_e32 v27, 0x440, v24
	v_lshlrev_b32_e32 v120, 4, v0
	v_lshrrev_b32_e32 v58, 5, v0
	v_mul_u32_u24_e32 v58, 0x110, v58
	v_and_b32_e32 v125, 31, v0
	v_lshl_add_u32 v58, v125, 3, v58
	v_add_u32_e32 v124, 0x1b400, v58
	v_mul_u32_u24_e32 v52, 0x110, v1
	v_add_u32_e32 v52, v52, v26
	v_add_u32_e32 v53, 0x1b400, v52
	v_add_u32_e32 v54, 0x1c500, v52
	v_add_u32_e32 v55, v27, v25
	v_add_u32_e32 v55, 0x1c500, v55
	v_mul_u32_u24_e32 v56, 0x110, v107
	v_add_u32_e32 v56, v56, v26
	v_add_u32_e32 v57, 0x8800, v56
	s_lshl_b32 s12, s2, 4
	s_add_i32 s3, s12, 0xfffff800
	s_cmpk_gt_i32 s2, 0x7f
	s_cselect_b64 s[6:7], -1, 0
	s_mov_b32 s48, 0
	s_mov_b32 s49, -1
	v_lshl_or_b32 v123, s2, 3, v128
	v_lshlrev_b32_e32 v123, 12, v123
	v_lshl_add_u32 v123, v126, 4, v123
	s_waitcnt lgkmcnt(0)
	s_cmpk_lt_i32 s2, 0x80
	s_cselect_b32 s38, s16, s18
	s_cselect_b32 s39, s17, s19
	s_cselect_b32 s40, s20, s24
	s_cselect_b32 s41, s21, s25
	s_cselect_b32 s13, s12, s3
	s_cselect_b32 s44, 0x3db504f3, 1.0
	s_lshl_b32 s13, s13, 9
	s_add_u32 s38, s38, s13
	s_addc_u32 s39, s39, 0
	global_load_dwordx4 v[2:5], v120, s[38:39] nt
	s_and_b32 s13, s2, 7
	s_lshl_b32 s14, s13, 13
	v_add_u32_e32 v125, s14, v120
	global_load_dwordx4 v[80:83], v125, s[40:41]
	s_add_i32 s13, s2, 1
	s_and_b32 s13, s13, 7
	s_lshl_b32 s14, s13, 13
	v_add_u32_e32 v125, s14, v120
	global_load_dwordx4 v[84:87], v125, s[40:41]
	s_add_i32 s13, s2, 2
	s_and_b32 s13, s13, 7
	s_lshl_b32 s14, s13, 13
	v_add_u32_e32 v125, s14, v120
	global_load_dwordx4 v[88:91], v125, s[40:41]
	s_add_i32 s13, s2, 3
	s_and_b32 s13, s13, 7
	s_lshl_b32 s14, s13, 13
	v_add_u32_e32 v125, s14, v120
	global_load_dwordx4 v[92:95], v125, s[40:41]
	s_add_i32 s13, s2, 4
	s_and_b32 s13, s13, 7
	s_lshl_b32 s14, s13, 13
	v_add_u32_e32 v125, s14, v120
	global_load_dwordx4 v[96:99], v125, s[40:41]
	s_add_i32 s13, s2, 5
	s_and_b32 s13, s13, 7
	s_lshl_b32 s14, s13, 13
	v_add_u32_e32 v125, s14, v120
	global_load_dwordx4 v[100:103], v125, s[40:41]
	s_add_i32 s13, s2, 6
	s_and_b32 s13, s13, 7
	s_lshl_b32 s14, s13, 13
	v_add_u32_e32 v125, s14, v120
	global_load_dwordx4 v[108:111], v125, s[40:41]
	s_add_i32 s13, s2, 7
	s_and_b32 s13, s13, 7
	s_lshl_b32 s14, s13, 13
	v_add_u32_e32 v125, s14, v120
	global_load_dwordx4 v[112:115], v125, s[40:41]
	global_load_dword v129, v106, s[32:33]
	global_load_dword v130, v106, s[30:31]
	s_and_b64 vcc, exec, s[6:7]
	s_cbranch_vccz .Lp_q
	v_cmp_gt_u32_e32 vcc, 32, v126
	v_mov_b32_e32 v198, 0x3db504f3
	v_mov_b32_e32 v125, s22
	v_mov_b32_e32 v104, s26
	v_cndmask_b32_e32 v198, 1.0, v198, vcc
	v_cndmask_b32_e32 v104, v104, v125, vcc
	v_mov_b32_e32 v125, s23
	v_mov_b32_e32 v105, s27
	v_cndmask_b32_e32 v105, v105, v125, vcc
	v_and_b32_e32 v196, 31, v126
	v_lshlrev_b32_e32 v196, 4, v196
	v_mov_b32_e32 v197, 0
	v_lshl_add_u64 v[104:105], v[104:105], 0, v[196:197]
	global_load_dwordx4 v[116:119], v[104:105], off
	v_lshlrev_b32_e32 v121, 14, v128
	v_lshl_add_u32 v121, v126, 4, v121
	s_and_b32 s13, s2, 15
	s_lshl_b32 s14, s13, 10
	s_add_u32 s46, s28, s14
	s_addc_u32 s47, s29, 0
	global_load_dwordx4 v[132:135], v121, s[46:47]
	s_add_i32 s13, s2, 1
	s_and_b32 s13, s13, 15
	s_lshl_b32 s14, s13, 10
	s_add_u32 s46, s28, s14
	s_addc_u32 s47, s29, 0
	global_load_dwordx4 v[136:139], v121, s[46:47]
	s_add_i32 s13, s2, 2
	s_and_b32 s13, s13, 15
	s_lshl_b32 s14, s13, 10
	s_add_u32 s46, s28, s14
	s_addc_u32 s47, s29, 0
	global_load_dwordx4 v[140:143], v121, s[46:47]
	s_add_i32 s13, s2, 3
	s_and_b32 s13, s13, 15
	s_lshl_b32 s14, s13, 10
	s_add_u32 s46, s28, s14
	s_addc_u32 s47, s29, 0
	global_load_dwordx4 v[144:147], v121, s[46:47]
	s_add_i32 s13, s2, 4
	s_and_b32 s13, s13, 15
	s_lshl_b32 s14, s13, 10
	s_add_u32 s46, s28, s14
	s_addc_u32 s47, s29, 0
	global_load_dwordx4 v[148:151], v121, s[46:47]
	s_add_i32 s13, s2, 5
	s_and_b32 s13, s13, 15
	s_lshl_b32 s14, s13, 10
	s_add_u32 s46, s28, s14
	s_addc_u32 s47, s29, 0
	global_load_dwordx4 v[152:155], v121, s[46:47]
	s_add_i32 s13, s2, 6
	s_and_b32 s13, s13, 15
	s_lshl_b32 s14, s13, 10
	s_add_u32 s46, s28, s14
	s_addc_u32 s47, s29, 0
	global_load_dwordx4 v[156:159], v121, s[46:47]
	s_add_i32 s13, s2, 7
	s_and_b32 s13, s13, 15
	s_lshl_b32 s14, s13, 10
	s_add_u32 s46, s28, s14
	s_addc_u32 s47, s29, 0
	global_load_dwordx4 v[160:163], v121, s[46:47]
	s_add_i32 s13, s2, 8
	s_and_b32 s13, s13, 15
	s_lshl_b32 s14, s13, 10
	s_add_u32 s46, s28, s14
	s_addc_u32 s47, s29, 0
	global_load_dwordx4 v[164:167], v121, s[46:47]
	s_add_i32 s13, s2, 9
	s_and_b32 s13, s13, 15
	s_lshl_b32 s14, s13, 10
	s_add_u32 s46, s28, s14
	s_addc_u32 s47, s29, 0
	global_load_dwordx4 v[168:171], v121, s[46:47]
	s_add_i32 s13, s2, 10
	s_and_b32 s13, s13, 15
	s_lshl_b32 s14, s13, 10
	s_add_u32 s46, s28, s14
	s_addc_u32 s47, s29, 0
	global_load_dwordx4 v[172:175], v121, s[46:47]
	s_add_i32 s13, s2, 11
	s_and_b32 s13, s13, 15
	s_lshl_b32 s14, s13, 10
	s_add_u32 s46, s28, s14
	s_addc_u32 s47, s29, 0
	global_load_dwordx4 v[176:179], v121, s[46:47]
	s_add_i32 s13, s2, 12
	s_and_b32 s13, s13, 15
	s_lshl_b32 s14, s13, 10
	s_add_u32 s46, s28, s14
	s_addc_u32 s47, s29, 0
	global_load_dwordx4 v[180:183], v121, s[46:47]
	s_add_i32 s13, s2, 13
	s_and_b32 s13, s13, 15
	s_lshl_b32 s14, s13, 10
	s_add_u32 s46, s28, s14
	s_addc_u32 s47, s29, 0
	global_load_dwordx4 v[184:187], v121, s[46:47]
	s_add_i32 s13, s2, 14
	s_and_b32 s13, s13, 15
	s_lshl_b32 s14, s13, 10
	s_add_u32 s46, s28, s14
	s_addc_u32 s47, s29, 0
	global_load_dwordx4 v[188:191], v121, s[46:47]
	s_add_i32 s13, s2, 15
	s_and_b32 s13, s13, 15
	s_lshl_b32 s14, s13, 10
	s_add_u32 s46, s28, s14
	s_addc_u32 s47, s29, 0
	global_load_dwordx4 v[192:195], v121, s[46:47]
	v_mul_u32_u24_e32 v59, 0x1040, v128
	v_lshl_add_u32 v59, v126, 2, v59
	v_add_u32_e32 v59, 0x11000, v59
	v_mul_u32_u24_e32 v76, 0x1100, v128
	v_lshl_add_u32 v76, v126, 3, v76
	v_add_u32_e32 v76, 0x8700, v76
	v_lshrrev_b32_e32 v77, 2, v126
	v_mul_u32_u24_e32 v77, 0x104, v77
	v_mul_u32_u24_e32 v125, 0x1040, v128
	v_add_u32_e32 v77, v77, v125
	v_and_b32_e32 v125, 3, v126
	v_lshl_add_u32 v77, v125, 6, v77
	v_add_u32_e32 v77, 0x11000, v77
	s_waitcnt vmcnt(27)
	v_cvt_pk_bf16_f32 v12, v2, v3
	v_cvt_pk_bf16_f32 v13, v4, v5
	ds_write_b64 v124, v[12:13]
	s_waitcnt vmcnt(26)
	v_cvt_pk_bf16_f32 v6, v80, v81
	v_cvt_pk_bf16_f32 v7, v82, v83
	s_and_b32 s13, s2, 7
	s_mul_i32 s14, s13, 0x1100
	v_add_u32_e32 v125, s14, v58
	ds_write_b64 v125, v[6:7]
	s_waitcnt vmcnt(25)
	v_cvt_pk_bf16_f32 v8, v84, v85
	v_cvt_pk_bf16_f32 v9, v86, v87
	s_add_i32 s13, s2, 1
	s_and_b32 s13, s13, 7
	s_mul_i32 s14, s13, 0x1100
	v_add_u32_e32 v10, s14, v58
	ds_write_b64 v10, v[8:9]
	s_waitcnt vmcnt(24)
	v_cvt_pk_bf16_f32 v6, v88, v89
	v_cvt_pk_bf16_f32 v7, v90, v91
	s_add_i32 s13, s2, 2
	s_and_b32 s13, s13, 7
	s_mul_i32 s14, s13, 0x1100
	v_add_u32_e32 v125, s14, v58
	ds_write_b64 v125, v[6:7]
	s_waitcnt vmcnt(23)
	v_cvt_pk_bf16_f32 v8, v92, v93
	v_cvt_pk_bf16_f32 v9, v94, v95
	s_add_i32 s13, s2, 3
	s_and_b32 s13, s13, 7
	s_mul_i32 s14, s13, 0x1100
	v_add_u32_e32 v10, s14, v58
	ds_write_b64 v10, v[8:9]
	s_waitcnt vmcnt(22)
	v_cvt_pk_bf16_f32 v6, v96, v97
	v_cvt_pk_bf16_f32 v7, v98, v99
	s_add_i32 s13, s2, 4
	s_and_b32 s13, s13, 7
	s_mul_i32 s14, s13, 0x1100
	v_add_u32_e32 v125, s14, v58
	ds_write_b64 v125, v[6:7]
	s_waitcnt vmcnt(21)
	v_cvt_pk_bf16_f32 v8, v100, v101
	v_cvt_pk_bf16_f32 v9, v102, v103
	s_add_i32 s13, s2, 5
	s_and_b32 s13, s13, 7
	s_mul_i32 s14, s13, 0x1100
	v_add_u32_e32 v10, s14, v58
	ds_write_b64 v10, v[8:9]
	s_waitcnt vmcnt(20)
	v_cvt_pk_bf16_f32 v6, v108, v109
	v_cvt_pk_bf16_f32 v7, v110, v111
	s_add_i32 s13, s2, 6
	s_and_b32 s13, s13, 7
	s_mul_i32 s14, s13, 0x1100
	v_add_u32_e32 v125, s14, v58
	ds_write_b64 v125, v[6:7]
	s_waitcnt vmcnt(19)
	v_cvt_pk_bf16_f32 v8, v112, v113
	v_cvt_pk_bf16_f32 v9, v114, v115
	s_add_i32 s13, s2, 7
	s_and_b32 s13, s13, 7
	s_mul_i32 s14, s13, 0x1100
	v_add_u32_e32 v10, s14, v58
	ds_write_b64 v10, v[8:9]
	s_waitcnt vmcnt(16)
	v_pk_mul_f32 v[116:117], v[198:199], v[116:117] op_sel_hi:[0,1]
	v_pk_mul_f32 v[118:119], v[198:199], v[118:119] op_sel_hi:[0,1]
	s_waitcnt vmcnt(15)
	v_mul_f32_e32 v6, v117, v133
	v_mul_f32_e32 v7, v119, v135
	v_fmac_f32_e32 v6, v116, v132
	v_fmac_f32_e32 v7, v118, v134
	s_and_b32 s13, s2, 15
	s_mul_i32 s14, s13, 0x104
	s_mul_i32 s15, s13, 0x110
	v_add_f32_e32 v6, v6, v7
	v_add_u32_e32 v125, s14, v59
	ds_write_b32 v125, v6
	v_cvt_pk_bf16_f32 v8, v132, v133
	v_cvt_pk_bf16_f32 v9, v134, v135
	v_add_u32_e32 v10, s15, v76
	s_mov_b64 exec, s[48:49]
	ds_write_b64 v10, v[8:9]
	s_mov_b64 exec, -1
	s_waitcnt vmcnt(14)
	v_mul_f32_e32 v11, v117, v137
	v_mul_f32_e32 v15, v119, v139
	v_fmac_f32_e32 v11, v116, v136
	v_fmac_f32_e32 v15, v118, v138
	s_add_i32 s13, s2, 1
	s_and_b32 s13, s13, 15
	s_mul_i32 s14, s13, 0x104
	s_mul_i32 s15, s13, 0x110
	v_add_f32_e32 v11, v11, v15
	v_add_u32_e32 v16, s14, v59
	ds_write_b32 v16, v11
	v_cvt_pk_bf16_f32 v12, v136, v137
	v_cvt_pk_bf16_f32 v13, v138, v139
	v_add_u32_e32 v14, s15, v76
	s_mov_b64 exec, s[48:49]
	ds_write_b64 v14, v[12:13]
	s_mov_b64 exec, -1
	s_waitcnt vmcnt(13)
	v_mul_f32_e32 v6, v117, v141
	v_mul_f32_e32 v7, v119, v143
	v_fmac_f32_e32 v6, v116, v140
	v_fmac_f32_e32 v7, v118, v142
	s_add_i32 s13, s2, 2
	s_and_b32 s13, s13, 15
	s_mul_i32 s14, s13, 0x104
	s_mul_i32 s15, s13, 0x110
	v_add_f32_e32 v6, v6, v7
	v_add_u32_e32 v125, s14, v59
	ds_write_b32 v125, v6
	v_cvt_pk_bf16_f32 v8, v140, v141
	v_cvt_pk_bf16_f32 v9, v142, v143
	v_add_u32_e32 v10, s15, v76
	s_mov_b64 exec, s[48:49]
	ds_write_b64 v10, v[8:9]
	s_mov_b64 exec, -1
	s_waitcnt vmcnt(12)
	v_mul_f32_e32 v11, v117, v145
	v_mul_f32_e32 v15, v119, v147
	v_fmac_f32_e32 v11, v116, v144
	v_fmac_f32_e32 v15, v118, v146
	s_add_i32 s13, s2, 3
	s_and_b32 s13, s13, 15
	s_mul_i32 s14, s13, 0x104
	s_mul_i32 s15, s13, 0x110
	v_add_f32_e32 v11, v11, v15
	v_add_u32_e32 v16, s14, v59
	ds_write_b32 v16, v11
	v_cvt_pk_bf16_f32 v12, v144, v145
	v_cvt_pk_bf16_f32 v13, v146, v147
	v_add_u32_e32 v14, s15, v76
	s_mov_b64 exec, s[48:49]
	ds_write_b64 v14, v[12:13]
	s_mov_b64 exec, -1
	s_waitcnt vmcnt(11)
	v_mul_f32_e32 v6, v117, v149
	v_mul_f32_e32 v7, v119, v151
	v_fmac_f32_e32 v6, v116, v148
	v_fmac_f32_e32 v7, v118, v150
	s_add_i32 s13, s2, 4
	s_and_b32 s13, s13, 15
	s_mul_i32 s14, s13, 0x104
	s_mul_i32 s15, s13, 0x110
	v_add_f32_e32 v6, v6, v7
	v_add_u32_e32 v125, s14, v59
	ds_write_b32 v125, v6
	v_cvt_pk_bf16_f32 v8, v148, v149
	v_cvt_pk_bf16_f32 v9, v150, v151
	v_add_u32_e32 v10, s15, v76
	s_mov_b64 exec, s[48:49]
	ds_write_b64 v10, v[8:9]
	s_mov_b64 exec, -1
	s_waitcnt vmcnt(10)
	v_mul_f32_e32 v11, v117, v153
	v_mul_f32_e32 v15, v119, v155
	v_fmac_f32_e32 v11, v116, v152
	v_fmac_f32_e32 v15, v118, v154
	s_add_i32 s13, s2, 5
	s_and_b32 s13, s13, 15
	s_mul_i32 s14, s13, 0x104
	s_mul_i32 s15, s13, 0x110
	v_add_f32_e32 v11, v11, v15
	v_add_u32_e32 v16, s14, v59
	ds_write_b32 v16, v11
	v_cvt_pk_bf16_f32 v12, v152, v153
	v_cvt_pk_bf16_f32 v13, v154, v155
	v_add_u32_e32 v14, s15, v76
	s_mov_b64 exec, s[48:49]
	ds_write_b64 v14, v[12:13]
	s_mov_b64 exec, -1
	s_waitcnt vmcnt(9)
	v_mul_f32_e32 v6, v117, v157
	v_mul_f32_e32 v7, v119, v159
	v_fmac_f32_e32 v6, v116, v156
	v_fmac_f32_e32 v7, v118, v158
	s_add_i32 s13, s2, 6
	s_and_b32 s13, s13, 15
	s_mul_i32 s14, s13, 0x104
	s_mul_i32 s15, s13, 0x110
	v_add_f32_e32 v6, v6, v7
	v_add_u32_e32 v125, s14, v59
	ds_write_b32 v125, v6
	v_cvt_pk_bf16_f32 v8, v156, v157
	v_cvt_pk_bf16_f32 v9, v158, v159
	v_add_u32_e32 v10, s15, v76
	s_mov_b64 exec, s[48:49]
	ds_write_b64 v10, v[8:9]
	s_mov_b64 exec, -1
	s_waitcnt vmcnt(8)
	v_mul_f32_e32 v11, v117, v161
	v_mul_f32_e32 v15, v119, v163
	v_fmac_f32_e32 v11, v116, v160
	v_fmac_f32_e32 v15, v118, v162
	s_add_i32 s13, s2, 7
	s_and_b32 s13, s13, 15
	s_mul_i32 s14, s13, 0x104
	s_mul_i32 s15, s13, 0x110
	v_add_f32_e32 v11, v11, v15
	v_add_u32_e32 v16, s14, v59
	ds_write_b32 v16, v11
	v_cvt_pk_bf16_f32 v12, v160, v161
	v_cvt_pk_bf16_f32 v13, v162, v163
	v_add_u32_e32 v14, s15, v76
	s_mov_b64 exec, s[48:49]
	ds_write_b64 v14, v[12:13]
	s_mov_b64 exec, -1
	s_waitcnt vmcnt(7)
	v_mul_f32_e32 v6, v117, v165
	v_mul_f32_e32 v7, v119, v167
	v_fmac_f32_e32 v6, v116, v164
	v_fmac_f32_e32 v7, v118, v166
	s_add_i32 s13, s2, 8
	s_and_b32 s13, s13, 15
	s_mul_i32 s14, s13, 0x104
	s_mul_i32 s15, s13, 0x110
	v_add_f32_e32 v6, v6, v7
	v_add_u32_e32 v125, s14, v59
	ds_write_b32 v125, v6
	v_cvt_pk_bf16_f32 v8, v164, v165
	v_cvt_pk_bf16_f32 v9, v166, v167
	v_add_u32_e32 v10, s15, v76
	s_mov_b64 exec, s[48:49]
	ds_write_b64 v10, v[8:9]
	s_mov_b64 exec, -1
	s_waitcnt vmcnt(6)
	v_mul_f32_e32 v11, v117, v169
	v_mul_f32_e32 v15, v119, v171
	v_fmac_f32_e32 v11, v116, v168
	v_fmac_f32_e32 v15, v118, v170
	s_add_i32 s13, s2, 9
	s_and_b32 s13, s13, 15
	s_mul_i32 s14, s13, 0x104
	s_mul_i32 s15, s13, 0x110
	v_add_f32_e32 v11, v11, v15
	v_add_u32_e32 v16, s14, v59
	ds_write_b32 v16, v11
	v_cvt_pk_bf16_f32 v12, v168, v169
	v_cvt_pk_bf16_f32 v13, v170, v171
	v_add_u32_e32 v14, s15, v76
	s_mov_b64 exec, s[48:49]
	ds_write_b64 v14, v[12:13]
	s_mov_b64 exec, -1
	s_waitcnt vmcnt(5)
	v_mul_f32_e32 v6, v117, v173
	v_mul_f32_e32 v7, v119, v175
	v_fmac_f32_e32 v6, v116, v172
	v_fmac_f32_e32 v7, v118, v174
	s_add_i32 s13, s2, 10
	s_and_b32 s13, s13, 15
	s_mul_i32 s14, s13, 0x104
	s_mul_i32 s15, s13, 0x110
	v_add_f32_e32 v6, v6, v7
	v_add_u32_e32 v125, s14, v59
	ds_write_b32 v125, v6
	v_cvt_pk_bf16_f32 v8, v172, v173
	v_cvt_pk_bf16_f32 v9, v174, v175
	v_add_u32_e32 v10, s15, v76
	s_mov_b64 exec, s[48:49]
	ds_write_b64 v10, v[8:9]
	s_mov_b64 exec, -1
	s_waitcnt vmcnt(4)
	v_mul_f32_e32 v11, v117, v177
	v_mul_f32_e32 v15, v119, v179
	v_fmac_f32_e32 v11, v116, v176
	v_fmac_f32_e32 v15, v118, v178
	s_add_i32 s13, s2, 11
	s_and_b32 s13, s13, 15
	s_mul_i32 s14, s13, 0x104
	s_mul_i32 s15, s13, 0x110
	v_add_f32_e32 v11, v11, v15
	v_add_u32_e32 v16, s14, v59
	ds_write_b32 v16, v11
	v_cvt_pk_bf16_f32 v12, v176, v177
	v_cvt_pk_bf16_f32 v13, v178, v179
	v_add_u32_e32 v14, s15, v76
	s_mov_b64 exec, s[48:49]
	ds_write_b64 v14, v[12:13]
	s_mov_b64 exec, -1
	s_waitcnt vmcnt(3)
	v_mul_f32_e32 v6, v117, v181
	v_mul_f32_e32 v7, v119, v183
	v_fmac_f32_e32 v6, v116, v180
	v_fmac_f32_e32 v7, v118, v182
	s_add_i32 s13, s2, 12
	s_and_b32 s13, s13, 15
	s_mul_i32 s14, s13, 0x104
	s_mul_i32 s15, s13, 0x110
	v_add_f32_e32 v6, v6, v7
	v_add_u32_e32 v125, s14, v59
	ds_write_b32 v125, v6
	v_cvt_pk_bf16_f32 v8, v180, v181
	v_cvt_pk_bf16_f32 v9, v182, v183
	v_add_u32_e32 v10, s15, v76
	s_mov_b64 exec, s[48:49]
	ds_write_b64 v10, v[8:9]
	s_mov_b64 exec, -1
	s_waitcnt vmcnt(2)
	v_mul_f32_e32 v11, v117, v185
	v_mul_f32_e32 v15, v119, v187
	v_fmac_f32_e32 v11, v116, v184
	v_fmac_f32_e32 v15, v118, v186
	s_add_i32 s13, s2, 13
	s_and_b32 s13, s13, 15
	s_mul_i32 s14, s13, 0x104
	s_mul_i32 s15, s13, 0x110
	v_add_f32_e32 v11, v11, v15
	v_add_u32_e32 v16, s14, v59
	ds_write_b32 v16, v11
	v_cvt_pk_bf16_f32 v12, v184, v185
	v_cvt_pk_bf16_f32 v13, v186, v187
	v_add_u32_e32 v14, s15, v76
	s_mov_b64 exec, s[48:49]
	ds_write_b64 v14, v[12:13]
	s_mov_b64 exec, -1
	s_waitcnt vmcnt(1)
	v_mul_f32_e32 v6, v117, v189
	v_mul_f32_e32 v7, v119, v191
	v_fmac_f32_e32 v6, v116, v188
	v_fmac_f32_e32 v7, v118, v190
	s_add_i32 s13, s2, 14
	s_and_b32 s13, s13, 15
	s_mul_i32 s14, s13, 0x104
	s_mul_i32 s15, s13, 0x110
	v_add_f32_e32 v6, v6, v7
	v_add_u32_e32 v125, s14, v59
	ds_write_b32 v125, v6
	v_cvt_pk_bf16_f32 v8, v188, v189
	v_cvt_pk_bf16_f32 v9, v190, v191
	v_add_u32_e32 v10, s15, v76
	s_mov_b64 exec, s[48:49]
	ds_write_b64 v10, v[8:9]
	s_mov_b64 exec, -1
	s_waitcnt vmcnt(0)
	v_mul_f32_e32 v11, v117, v193
	v_mul_f32_e32 v15, v119, v195
	v_fmac_f32_e32 v11, v116, v192
	v_fmac_f32_e32 v15, v118, v194
	s_add_i32 s13, s2, 15
	s_and_b32 s13, s13, 15
	s_mul_i32 s14, s13, 0x104
	s_mul_i32 s15, s13, 0x110
	v_add_f32_e32 v11, v11, v15
	v_add_u32_e32 v16, s14, v59
	ds_write_b32 v16, v11
	v_cvt_pk_bf16_f32 v12, v192, v193
	v_cvt_pk_bf16_f32 v13, v194, v195
	v_add_u32_e32 v14, s15, v76
	s_mov_b64 exec, s[48:49]
	ds_write_b64 v14, v[12:13]
	s_mov_b64 exec, -1
	s_waitcnt lgkmcnt(0)
	ds_read2_b32 v[60:61], v77 offset0:0 offset1:1
	ds_read2_b32 v[62:63], v77 offset0:2 offset1:3
	ds_read2_b32 v[64:65], v77 offset0:4 offset1:5
	ds_read2_b32 v[66:67], v77 offset0:6 offset1:7
	ds_read2_b32 v[68:69], v77 offset0:8 offset1:9
	ds_read2_b32 v[70:71], v77 offset0:10 offset1:11
	ds_read2_b32 v[72:73], v77 offset0:12 offset1:13
	ds_read2_b32 v[74:75], v77 offset0:14 offset1:15
	s_waitcnt lgkmcnt(0)
	v_add_f32_e32 v78, 0, v60
	v_add_f32_e32 v78, v78, v61
	v_add_f32_e32 v78, v78, v62
	v_add_f32_e32 v78, v78, v63
	v_add_f32_e32 v78, v78, v64
	v_add_f32_e32 v78, v78, v65
	v_add_f32_e32 v78, v78, v66
	v_add_f32_e32 v78, v78, v67
	v_add_f32_e32 v78, v78, v68
	v_add_f32_e32 v78, v78, v69
	v_add_f32_e32 v78, v78, v70
	v_add_f32_e32 v78, v78, v71
	v_add_f32_e32 v78, v78, v72
	v_add_f32_e32 v78, v78, v73
	v_add_f32_e32 v78, v78, v74
	v_add_f32_e32 v78, v78, v75
	s_nop 1
	v_add_f32_dpp v78, v78, v78 quad_perm:[1,0,3,2] row_mask:0xf bank_mask:0xf bound_ctrl:1
	s_nop 1
	v_add_f32_dpp v78, v78, v78 quad_perm:[2,3,0,1] row_mask:0xf bank_mask:0xf bound_ctrl:1
	v_lshlrev_b32_e32 v79, 4, v1
	ds_bpermute_b32 v78, v79, v78
	s_waitcnt lgkmcnt(0)
	s_barrier
	ds_read_b128 v[28:31], v53
	ds_read_b128 v[60:63], v56
	ds_read_b128 v[32:35], v53 offset:64
	ds_read_b128 v[64:67], v56 offset:64
	ds_read_b128 v[36:39], v53 offset:128
	ds_read_b128 v[68:71], v56 offset:128
	ds_read_b128 v[40:43], v53 offset:192
	ds_read_b128 v[72:75], v56 offset:192
	s_waitcnt lgkmcnt(6)
	v_mfma_f32_16x16x32_bf16 v[18:21], v[28:31], v[60:63], 0
	s_waitcnt lgkmcnt(4)
	v_mfma_f32_16x16x32_bf16 v[18:21], v[32:35], v[64:67], v[18:21]
	s_waitcnt lgkmcnt(2)
	v_mfma_f32_16x16x32_bf16 v[18:21], v[36:39], v[68:71], v[18:21]
	s_waitcnt lgkmcnt(0)
	v_mfma_f32_16x16x32_bf16 v[18:21], v[40:43], v[72:75], v[18:21]
	s_nop 7
	v_mul_f32_e32 v18, s44, v18
	v_mul_f32_e32 v19, s44, v19
	v_mul_f32_e32 v20, s44, v20
	v_mul_f32_e32 v21, s44, v21
	v_cvt_pk_bf16_f32 v18, v18, v18
	v_cvt_pk_bf16_f32 v19, v19, v19
	v_cvt_pk_bf16_f32 v20, v20, v20
	v_cvt_pk_bf16_f32 v21, v21, v21
	ds_write_b16 v55, v18
	ds_write_b16 v55, v19 offset:272
	ds_write_b16 v55, v20 offset:544
	ds_write_b16 v55, v21 offset:816
	s_waitcnt lgkmcnt(0)
	s_barrier
	ds_read_b128 v[28:31], v54
	ds_read_b128 v[60:63], v57
	ds_read_b128 v[32:35], v54 offset:64
	ds_read_b128 v[64:67], v57 offset:64
	ds_read_b128 v[36:39], v54 offset:128
	ds_read_b128 v[68:71], v57 offset:128
	ds_read_b128 v[40:43], v54 offset:192
	ds_read_b128 v[72:75], v57 offset:192
	s_waitcnt lgkmcnt(6)
	v_mfma_f32_16x16x32_bf16 v[18:21], v[28:31], v[60:63], 0
	s_waitcnt lgkmcnt(4)
	v_mfma_f32_16x16x32_bf16 v[18:21], v[32:35], v[64:67], v[18:21]
	s_waitcnt lgkmcnt(2)
	v_mfma_f32_16x16x32_bf16 v[18:21], v[36:39], v[68:71], v[18:21]
	s_waitcnt lgkmcnt(0)
	v_mfma_f32_16x16x32_bf16 v[18:21], v[40:43], v[72:75], v[18:21]
	s_nop 4
	v_add_f32_e32 v34, v130, v78
	v_lshl_or_b32 v30, v24, 2, s3
	v_lshlrev_b32_e32 v30, 9, v30
	v_add_u32_e32 v30, v30, v106
	v_add_u32_e32 v37, v27, v25
	v_add_u32_e32 v37, 0x19200, v37
	v_add_f32_e32 v80, v34, v18
	v_add_f32_e32 v81, v34, v19
	v_add_f32_e32 v82, v34, v20
	v_add_f32_e32 v83, v34, v21
	s_waitcnt lgkmcnt(0)
	global_store_dword v30, v80, s[68:69] sc1
	global_store_dword v30, v81, s[68:69] offset:512 sc1
	global_store_dword v30, v82, s[68:69] offset:1024 sc1
	global_store_dword v30, v83, s[68:69] offset:1536 sc1
	v_add_f32_e32 v84, v80, v80
	v_add_f32_e32 v85, v81, v81
	v_add_f32_e32 v86, v82, v82
	v_add_f32_e32 v87, v83, v83
	v_mul_f32_e32 v84, 0x3fb8aa3b, v84
	v_mul_f32_e32 v85, 0x3fb8aa3b, v85
	v_mul_f32_e32 v86, 0x3fb8aa3b, v86
	v_mul_f32_e32 v87, 0x3fb8aa3b, v87
	v_exp_f32_e32 v84, v84
	v_exp_f32_e32 v85, v85
	v_exp_f32_e32 v86, v86
	v_exp_f32_e32 v87, v87
	v_add_f32_e32 v84, 1.0, v84
	v_add_f32_e32 v85, 1.0, v85
	v_add_f32_e32 v86, 1.0, v86
	v_add_f32_e32 v87, 1.0, v87
	v_rcp_f32_e32 v84, v84
	v_rcp_f32_e32 v85, v85
	v_rcp_f32_e32 v86, v86
	v_rcp_f32_e32 v87, v87
	v_fma_f32 v84, v84, -2.0, 1.0
	v_fma_f32 v85, v85, -2.0, 1.0
	v_fma_f32 v86, v86, -2.0, 1.0
	v_fma_f32 v87, v87, -2.0, 1.0
	v_fma_f32 v88, -v84, v84, 1.0
	v_fma_f32 v89, -v85, v85, 1.0
	v_fma_f32 v90, -v86, v86, 1.0
	v_fma_f32 v91, -v87, v87, 1.0
	v_mul_f32_e32 v96, v129, v84
	v_mul_f32_e32 v97, v129, v85
	v_mul_f32_e32 v98, v129, v86
	v_mul_f32_e32 v99, v129, v87
	v_mul_f32_e32 v88, v129, v88
	v_mul_f32_e32 v89, v129, v89
	v_mul_f32_e32 v90, v129, v90
	v_mul_f32_e32 v91, v129, v91
	v_mul_f32_e64 v92, v84, -v88
	v_mul_f32_e64 v93, v85, -v89
	v_mul_f32_e64 v94, v86, -v90
	v_mul_f32_e64 v95, v87, -v91
	v_add_f32_dpp v100, v96, v96 quad_perm:[1,0,3,2] row_mask:0xf bank_mask:0xf
	v_add_f32_dpp v101, v97, v97 quad_perm:[1,0,3,2] row_mask:0xf bank_mask:0xf
	v_add_f32_dpp v102, v98, v98 quad_perm:[1,0,3,2] row_mask:0xf bank_mask:0xf
	v_add_f32_dpp v103, v99, v99 quad_perm:[1,0,3,2] row_mask:0xf bank_mask:0xf
	v_add_f32_dpp v96, v100, v100 quad_perm:[2,3,0,1] row_mask:0xf bank_mask:0xf
	v_add_f32_dpp v97, v101, v101 quad_perm:[2,3,0,1] row_mask:0xf bank_mask:0xf
	v_add_f32_dpp v98, v102, v102 quad_perm:[2,3,0,1] row_mask:0xf bank_mask:0xf
	v_add_f32_dpp v99, v103, v103 quad_perm:[2,3,0,1] row_mask:0xf bank_mask:0xf
	v_cvt_pk_bf16_f32 v88, v88, v88
	v_cvt_pk_bf16_f32 v89, v89, v89
	v_cvt_pk_bf16_f32 v90, v90, v90
	v_cvt_pk_bf16_f32 v91, v91, v91
	v_add_f32_dpp v100, v96, v96 row_half_mirror row_mask:0xf bank_mask:0xf
	v_add_f32_dpp v101, v97, v97 row_half_mirror row_mask:0xf bank_mask:0xf
	v_add_f32_dpp v102, v98, v98 row_half_mirror row_mask:0xf bank_mask:0xf
	v_add_f32_dpp v103, v99, v99 row_half_mirror row_mask:0xf bank_mask:0xf
	v_cvt_pk_bf16_f32 v92, v92, v92
	v_cvt_pk_bf16_f32 v93, v93, v93
	v_cvt_pk_bf16_f32 v94, v94, v94
	v_cvt_pk_bf16_f32 v95, v95, v95
	v_add_f32_dpp v96, v100, v100 row_mirror row_mask:0xf bank_mask:0xf
	v_add_f32_dpp v97, v101, v101 row_mirror row_mask:0xf bank_mask:0xf
	v_add_f32_dpp v98, v102, v102 row_mirror row_mask:0xf bank_mask:0xf
	v_add_f32_dpp v99, v103, v103 row_mirror row_mask:0xf bank_mask:0xf
	ds_write_b16 v37, v88
	ds_write_b16 v37, v89 offset:272
	ds_write_b16 v37, v90 offset:544
	ds_write_b16 v37, v91 offset:816
	ds_write_b16 v37, v92 offset:4352
	ds_write_b16 v37, v93 offset:4624
	ds_write_b16 v37, v94 offset:4896
	ds_write_b16 v37, v95 offset:5168
	v_mov_b32_e32 v32, 0x1d800
	v_lshl_or_b32 v32, v128, 6, v32
	v_add_u32_e32 v32, v32, v26
	v_cmp_eq_u32_e32 vcc, 0, v1
	s_and_saveexec_b64 s[8:9], vcc
	ds_write_b128 v32, v[96:99]
	s_or_b64 exec, exec, s[8:9]
	s_branch .LBB0_28
.Lp_q:
	v_lshrrev_b32_e32 v122, 5, v0
	v_lshlrev_b32_e32 v122, 10, v122
	v_and_b32_e32 v125, 31, v0
	v_lshl_add_u32 v122, v125, 4, v122
	s_and_b32 s13, s2, 7
	s_lshl_b32 s14, s13, 14
	v_add_u32_e32 v125, s14, v122
	global_load_dwordx4 v[132:135], v125, s[28:29]
	s_add_i32 s13, s2, 1
	s_and_b32 s13, s13, 7
	s_lshl_b32 s14, s13, 14
	v_add_u32_e32 v125, s14, v122
	global_load_dwordx4 v[136:139], v125, s[28:29]
	s_add_i32 s13, s2, 2
	s_and_b32 s13, s13, 7
	s_lshl_b32 s14, s13, 14
	v_add_u32_e32 v125, s14, v122
	global_load_dwordx4 v[140:143], v125, s[28:29]
	s_add_i32 s13, s2, 3
	s_and_b32 s13, s13, 7
	s_lshl_b32 s14, s13, 14
	v_add_u32_e32 v125, s14, v122
	global_load_dwordx4 v[144:147], v125, s[28:29]
	s_add_i32 s13, s2, 4
	s_and_b32 s13, s13, 7
	s_lshl_b32 s14, s13, 14
	v_add_u32_e32 v125, s14, v122
	global_load_dwordx4 v[148:151], v125, s[28:29]
	s_add_i32 s13, s2, 5
	s_and_b32 s13, s13, 7
	s_lshl_b32 s14, s13, 14
	v_add_u32_e32 v125, s14, v122
	global_load_dwordx4 v[152:155], v125, s[28:29]
	s_add_i32 s13, s2, 6
	s_and_b32 s13, s13, 7
	s_lshl_b32 s14, s13, 14
	v_add_u32_e32 v125, s14, v122
	global_load_dwordx4 v[156:159], v125, s[28:29]
	s_add_i32 s13, s2, 7
	s_and_b32 s13, s13, 7
	s_lshl_b32 s14, s13, 14
	v_add_u32_e32 v125, s14, v122
	global_load_dwordx4 v[160:163], v125, s[28:29]
	s_waitcnt vmcnt(18)
	v_cvt_pk_bf16_f32 v12, v2, v3
	v_cvt_pk_bf16_f32 v13, v4, v5
	ds_write_b64 v124, v[12:13]
	s_waitcnt vmcnt(17)
	v_cvt_pk_bf16_f32 v6, v80, v81
	v_cvt_pk_bf16_f32 v7, v82, v83
	s_and_b32 s13, s2, 7
	s_mul_i32 s14, s13, 0x1100
	v_add_u32_e32 v125, s14, v58
	ds_write_b64 v125, v[6:7]
	s_waitcnt vmcnt(16)
	v_cvt_pk_bf16_f32 v8, v84, v85
	v_cvt_pk_bf16_f32 v9, v86, v87
	s_add_i32 s13, s2, 1
	s_and_b32 s13, s13, 7
	s_mul_i32 s14, s13, 0x1100
	v_add_u32_e32 v10, s14, v58
	ds_write_b64 v10, v[8:9]
	s_waitcnt vmcnt(15)
	v_cvt_pk_bf16_f32 v6, v88, v89
	v_cvt_pk_bf16_f32 v7, v90, v91
	s_add_i32 s13, s2, 2
	s_and_b32 s13, s13, 7
	s_mul_i32 s14, s13, 0x1100
	v_add_u32_e32 v125, s14, v58
	ds_write_b64 v125, v[6:7]
	s_waitcnt vmcnt(14)
	v_cvt_pk_bf16_f32 v8, v92, v93
	v_cvt_pk_bf16_f32 v9, v94, v95
	s_add_i32 s13, s2, 3
	s_and_b32 s13, s13, 7
	s_mul_i32 s14, s13, 0x1100
	v_add_u32_e32 v10, s14, v58
	ds_write_b64 v10, v[8:9]
	s_waitcnt vmcnt(13)
	v_cvt_pk_bf16_f32 v6, v96, v97
	v_cvt_pk_bf16_f32 v7, v98, v99
	s_add_i32 s13, s2, 4
	s_and_b32 s13, s13, 7
	s_mul_i32 s14, s13, 0x1100
	v_add_u32_e32 v125, s14, v58
	ds_write_b64 v125, v[6:7]
	s_waitcnt vmcnt(12)
	v_cvt_pk_bf16_f32 v8, v100, v101
	v_cvt_pk_bf16_f32 v9, v102, v103
	s_add_i32 s13, s2, 5
	s_and_b32 s13, s13, 7
	s_mul_i32 s14, s13, 0x1100
	v_add_u32_e32 v10, s14, v58
	ds_write_b64 v10, v[8:9]
	s_waitcnt vmcnt(11)
	v_cvt_pk_bf16_f32 v6, v108, v109
	v_cvt_pk_bf16_f32 v7, v110, v111
	s_add_i32 s13, s2, 6
	s_and_b32 s13, s13, 7
	s_mul_i32 s14, s13, 0x1100
	v_add_u32_e32 v125, s14, v58
	ds_write_b64 v125, v[6:7]
	s_waitcnt vmcnt(10)
	v_cvt_pk_bf16_f32 v8, v112, v113
	v_cvt_pk_bf16_f32 v9, v114, v115
	s_add_i32 s13, s2, 7
	s_and_b32 s13, s13, 7
	s_mul_i32 s14, s13, 0x1100
	v_add_u32_e32 v10, s14, v58
	ds_write_b64 v10, v[8:9]
	s_waitcnt vmcnt(7)
	v_cvt_pk_bf16_f32 v6, v132, v133
	v_cvt_pk_bf16_f32 v7, v134, v135
	s_and_b32 s13, s2, 7
	s_mul_i32 s14, s13, 0x1100
	s_add_i32 s14, s14, 34816
	v_add_u32_e32 v125, s14, v58
	ds_write_b64 v125, v[6:7]
	s_waitcnt vmcnt(6)
	v_cvt_pk_bf16_f32 v8, v136, v137
	v_cvt_pk_bf16_f32 v9, v138, v139
	s_add_i32 s13, s2, 1
	s_and_b32 s13, s13, 7
	s_mul_i32 s14, s13, 0x1100
	s_add_i32 s14, s14, 34816
	v_add_u32_e32 v10, s14, v58
	ds_write_b64 v10, v[8:9]
	s_waitcnt vmcnt(5)
	v_cvt_pk_bf16_f32 v6, v140, v141
	v_cvt_pk_bf16_f32 v7, v142, v143
	s_add_i32 s13, s2, 2
	s_and_b32 s13, s13, 7
	s_mul_i32 s14, s13, 0x1100
	s_add_i32 s14, s14, 34816
	v_add_u32_e32 v125, s14, v58
	ds_write_b64 v125, v[6:7]
	s_waitcnt vmcnt(4)
	v_cvt_pk_bf16_f32 v8, v144, v145
	v_cvt_pk_bf16_f32 v9, v146, v147
	s_add_i32 s13, s2, 3
	s_and_b32 s13, s13, 7
	s_mul_i32 s14, s13, 0x1100
	s_add_i32 s14, s14, 34816
	v_add_u32_e32 v10, s14, v58
	ds_write_b64 v10, v[8:9]
	s_waitcnt vmcnt(3)
	v_cvt_pk_bf16_f32 v6, v148, v149
	v_cvt_pk_bf16_f32 v7, v150, v151
	s_add_i32 s13, s2, 4
	s_and_b32 s13, s13, 7
	s_mul_i32 s14, s13, 0x1100
	s_add_i32 s14, s14, 34816
	v_add_u32_e32 v125, s14, v58
	ds_write_b64 v125, v[6:7]
	s_waitcnt vmcnt(2)
	v_cvt_pk_bf16_f32 v8, v152, v153
	v_cvt_pk_bf16_f32 v9, v154, v155
	s_add_i32 s13, s2, 5
	s_and_b32 s13, s13, 7
	s_mul_i32 s14, s13, 0x1100
	s_add_i32 s14, s14, 34816
	v_add_u32_e32 v10, s14, v58
	ds_write_b64 v10, v[8:9]
	s_waitcnt vmcnt(1)
	v_cvt_pk_bf16_f32 v6, v156, v157
	v_cvt_pk_bf16_f32 v7, v158, v159
	s_add_i32 s13, s2, 6
	s_and_b32 s13, s13, 7
	s_mul_i32 s14, s13, 0x1100
	s_add_i32 s14, s14, 34816
	v_add_u32_e32 v125, s14, v58
	ds_write_b64 v125, v[6:7]
	s_waitcnt vmcnt(0)
	v_cvt_pk_bf16_f32 v8, v160, v161
	v_cvt_pk_bf16_f32 v9, v162, v163
	s_add_i32 s13, s2, 7
	s_and_b32 s13, s13, 7
	s_mul_i32 s14, s13, 0x1100
	s_add_i32 s14, s14, 34816
	v_add_u32_e32 v10, s14, v58
	ds_write_b64 v10, v[8:9]
	s_waitcnt lgkmcnt(0)
	s_barrier
	v_lshl_add_u32 v123, v128, 1, s12
	v_lshlrev_b32_e32 v123, 12, v123
	v_lshl_add_u32 v123, v126, 4, v123
	v_add_u32_e32 v125, 0x1000, v123
	global_load_dwordx4 v[2:5], v123, s[34:35] nt
	global_load_dwordx4 v[6:9], v123, s[34:35] offset:1024 nt
	global_load_dwordx4 v[10:13], v123, s[34:35] offset:2048 nt
	global_load_dwordx4 v[14:17], v123, s[34:35] offset:3072 nt
	global_load_dwordx4 v[132:135], v125, s[34:35] nt
	global_load_dwordx4 v[136:139], v125, s[34:35] offset:1024 nt
	global_load_dwordx4 v[140:143], v125, s[34:35] offset:2048 nt
	global_load_dwordx4 v[144:147], v125, s[34:35] offset:3072 nt
	ds_read_b128 v[28:31], v53
	ds_read_b128 v[60:63], v56
	ds_read_b128 v[32:35], v53 offset:64
	ds_read_b128 v[64:67], v56 offset:64
	ds_read_b128 v[36:39], v53 offset:128
	ds_read_b128 v[68:71], v56 offset:128
	ds_read_b128 v[40:43], v53 offset:192
	ds_read_b128 v[72:75], v56 offset:192
	s_waitcnt lgkmcnt(6)
	v_mfma_f32_16x16x32_bf16 v[18:21], v[28:31], v[60:63], 0
	s_waitcnt lgkmcnt(4)
	v_mfma_f32_16x16x32_bf16 v[18:21], v[32:35], v[64:67], v[18:21]
	s_waitcnt lgkmcnt(2)
	v_mfma_f32_16x16x32_bf16 v[18:21], v[36:39], v[68:71], v[18:21]
	s_waitcnt lgkmcnt(0)
	v_mfma_f32_16x16x32_bf16 v[18:21], v[40:43], v[72:75], v[18:21]
	s_nop 7
	v_mul_f32_e32 v18, s44, v18
	v_mul_f32_e32 v19, s44, v19
	v_mul_f32_e32 v20, s44, v20
	v_mul_f32_e32 v21, s44, v21
	v_cvt_pk_bf16_f32 v18, v18, v18
	v_cvt_pk_bf16_f32 v19, v19, v19
	v_cvt_pk_bf16_f32 v20, v20, v20
	v_cvt_pk_bf16_f32 v21, v21, v21
	ds_write_b16 v55, v18
	ds_write_b16 v55, v19 offset:272
	ds_write_b16 v55, v20 offset:544
	ds_write_b16 v55, v21 offset:816
	s_waitcnt lgkmcnt(0)
	s_barrier
	ds_read_b128 v[28:31], v54
	ds_read_b128 v[60:63], v57
	ds_read_b128 v[32:35], v54 offset:64
	ds_read_b128 v[64:67], v57 offset:64
	ds_read_b128 v[36:39], v54 offset:128
	ds_read_b128 v[68:71], v57 offset:128
	ds_read_b128 v[40:43], v54 offset:192
	ds_read_b128 v[72:75], v57 offset:192
	s_waitcnt lgkmcnt(6)
	v_mfma_f32_16x16x32_bf16 v[18:21], v[28:31], v[60:63], 0
	s_waitcnt lgkmcnt(4)
	v_mfma_f32_16x16x32_bf16 v[18:21], v[32:35], v[64:67], v[18:21]
	s_waitcnt lgkmcnt(2)
	v_mfma_f32_16x16x32_bf16 v[18:21], v[36:39], v[68:71], v[18:21]
	s_waitcnt lgkmcnt(0)
	v_mfma_f32_16x16x32_bf16 v[18:21], v[40:43], v[72:75], v[18:21]
	s_mov_b64 s[4:5], s[66:67]
	v_lshl_or_b32 v26, v24, 2, s12
	v_mov_b32_e32 v107, 0
	v_ashrrev_i32_e32 v27, 31, v26
	v_lshlrev_b64 v[28:29], 9, v[26:27]
	s_waitcnt lgkmcnt(0)
	v_lshl_add_u64 v[30:31], s[4:5], 0, v[106:107]
	v_lshl_add_u64 v[28:29], v[30:31], 0, v[28:29]
	v_mul_u32_u24_e32 v24, 0x440, v24
	s_mov_b32 s4, 0x19200
	global_store_dword v[28:29], v18, off sc1
	v_add3_u32 v28, v24, v25, s4
	v_mul_f32_e32 v24, v18, v18
	v_cvt_pk_bf16_f32 v27, v18, s0
	v_cvt_pk_bf16_f32 v24, v24, s0
	ds_write_b16 v28, v27
	ds_write_b16 v28, v24 offset:4352
	v_max3_f32 v27, |v18|, 0, |v19|
	v_or_b32_e32 v24, 1, v26
	v_cvt_pk_bf16_f32 v18, v19, s0
	v_ashrrev_i32_e32 v25, 31, v24
	ds_write_b16 v28, v18 offset:272
	v_mul_f32_e32 v18, v19, v19
	v_lshlrev_b64 v[24:25], 9, v[24:25]
	v_cvt_pk_bf16_f32 v18, v18, s0
	v_lshl_add_u64 v[24:25], v[30:31], 0, v[24:25]
	ds_write_b16 v28, v18 offset:4624
	v_or_b32_e32 v18, 2, v26
	global_store_dword v[24:25], v19, off sc1
	v_ashrrev_i32_e32 v19, 31, v18
	v_lshlrev_b64 v[18:19], 9, v[18:19]
	v_lshl_add_u64 v[18:19], v[30:31], 0, v[18:19]
	global_store_dword v[18:19], v20, off sc1
	v_cvt_pk_bf16_f32 v18, v20, s0
	ds_write_b16 v28, v18 offset:544
	v_mul_f32_e32 v18, v20, v20
	v_cvt_pk_bf16_f32 v18, v18, s0
	ds_write_b16 v28, v18 offset:4896
	v_or_b32_e32 v18, 3, v26
	v_ashrrev_i32_e32 v19, 31, v18
	v_lshlrev_b64 v[18:19], 9, v[18:19]
	v_lshl_add_u64 v[18:19], v[30:31], 0, v[18:19]
	global_store_dword v[18:19], v21, off sc1
	v_cvt_pk_bf16_f32 v18, v21, s0
	ds_write_b16 v28, v18 offset:816
	v_mul_f32_e32 v18, v21, v21
	v_cvt_pk_bf16_f32 v18, v18, s0
	v_max3_f32 v20, v27, |v20|, |v21|
	ds_write_b16 v28, v18 offset:5168
	v_mov_b32_e32 v18, v107
	v_mov_b32_e32 v19, v107
	v_cmp_eq_u32_e32 vcc, 0, v126
	v_mov_b32_dpp v18, v20 quad_perm:[1,0,3,2] row_mask:0xf bank_mask:0xf
	v_max_f32_e32 v18, v18, v18
	v_max_f32_e32 v18, v20, v18
	s_nop 1
	v_mov_b32_dpp v19, v18 quad_perm:[2,3,0,1] row_mask:0xf bank_mask:0xf
	v_max_f32_e32 v19, v19, v19
	v_max_f32_e32 v18, v18, v19
	v_mov_b32_e32 v19, v107
	s_nop 1
	v_mov_b32_dpp v19, v18 row_half_mirror row_mask:0xf bank_mask:0xf
	v_max_f32_e32 v19, v19, v19
	v_max_f32_e32 v18, v18, v19
	v_mov_b32_e32 v19, v107
	s_nop 1
	v_mov_b32_dpp v19, v18 row_mirror row_mask:0xf bank_mask:0xf
	v_max_f32_e32 v19, v19, v19
	v_max_f32_e32 v18, v18, v19
	s_nop 0
	v_readlane_b32 s8, v18, 0
	v_readlane_b32 s9, v18, 16
	v_readlane_b32 s10, v18, 32
	v_readlane_b32 s11, v18, 48
	v_and_b32_e32 v18, 0x7fffffff, v129
	s_nop 1
	v_add_f32_dpp v18, v18, |v129| quad_perm:[1,0,3,2] row_mask:0xf bank_mask:0xf bound_ctrl:1
	s_nop 1
	v_add_f32_dpp v18, v18, v18 quad_perm:[2,3,0,1] row_mask:0xf bank_mask:0xf bound_ctrl:1
	s_nop 1
	v_add_f32_dpp v18, v18, v18 row_half_mirror row_mask:0xf bank_mask:0xf bound_ctrl:1
	s_nop 1
	v_mov_b32_dpp v107, v18 row_mirror row_mask:0xf bank_mask:0xf
	s_and_saveexec_b64 s[4:5], vcc
	s_cbranch_execz .LBB0_27
	v_mov_b32_e32 v19, 0x1d800
	v_lshl_or_b32 v20, v128, 6, v19
	v_add_f32_e32 v19, v18, v107
	v_max_f32_e64 v18, s11, s11
	v_max_f32_e64 v21, s10, s10
	v_max_f32_e32 v18, v21, v18
	v_mov_b32_e32 v21, s9
	v_max3_f32 v18, s8, v21, v18
	ds_write_b64 v20, v[18:19]

.LBB0_28:
	s_mov_b64 s[8:9], -1
	s_and_b64 vcc, exec, s[6:7]
	s_waitcnt lgkmcnt(0)
	s_barrier
	s_cbranch_vccz .LBB0_34
	v_cmp_gt_u32_e32 vcc, 16, v0
	s_and_saveexec_b64 s[4:5], vcc
	s_cbranch_execz .LBB0_31
	v_or_b32_e32 v18, 0x1d800, v127
	v_add_u32_e32 v19, 0x1d840, v127
	v_add_u32_e32 v20, 0x1d880, v127
	v_add_u32_e32 v21, 0x1d8c0, v127
	v_add_u32_e32 v24, 0x1d900, v127
	v_add_u32_e32 v25, 0x1d940, v127
	v_add_u32_e32 v26, 0x1d980, v127
	v_add_u32_e32 v27, 0x1d9c0, v127
	ds_read_b32 v18, v18
	ds_read_b32 v19, v19
	ds_read_b32 v20, v20
	ds_read_b32 v21, v21
	ds_read_b32 v24, v24
	ds_read_b32 v25, v25
	ds_read_b32 v26, v26
	ds_read_b32 v27, v27
	s_waitcnt lgkmcnt(7)
	v_add_f32_e32 v18, 0, v18
	s_waitcnt lgkmcnt(6)
	v_add_f32_e32 v18, v18, v19
	s_waitcnt lgkmcnt(5)
	v_add_f32_e32 v18, v18, v20
	s_waitcnt lgkmcnt(4)
	v_add_f32_e32 v18, v18, v21
	s_mov_b64 s[6:7], s[64:65]
	s_waitcnt lgkmcnt(0)
	v_add_f32_e32 v18, v18, v24
	v_add_f32_e32 v18, v18, v25
	v_add_f32_e32 v18, v18, v26
	v_add_f32_e32 v20, v18, v27
	v_or_b32_e32 v18, s3, v0
	v_ashrrev_i32_e32 v19, 31, v18
	v_lshl_add_u64 v[18:19], v[18:19], 2, s[6:7]
	global_store_dword v[18:19], v20, off sc1
.LBB0_31:
	s_or_b64 exec, exec, s[4:5]
	s_movk_i32 s4, 0x200
	v_cmp_gt_u32_e32 vcc, s4, v0
	s_and_saveexec_b64 s[4:5], vcc
	s_cbranch_execz .LBB0_33
	s_mov_b64 s[6:7], s[62:63]
	s_ashr_i32 s3, s3, 9
	v_lshrrev_b32_e32 v20, 8, v0
	v_and_or_b32 v18, s3, -2, v20
	v_ashrrev_i32_e32 v19, 31, v18
	v_lshlrev_b64 v[18:19], 18, v[18:19]
	s_lshl_b32 s3, s2, 12
	s_waitcnt lgkmcnt(0)
	v_lshl_add_u64 v[18:19], s[6:7], 0, v[18:19]
	s_and_b32 s6, s3, 0x3f000
	s_mov_b32 s7, 0
	v_lshl_add_u64 v[24:25], v[18:19], 0, s[6:7]
	v_mul_u32_u24_e32 v18, 0x1100, v20
	s_movk_i32 s3, 0x110
	v_mad_u32_u24 v18, v1, s3, v18
	v_and_b32_e32 v19, 0xf0, v0
	s_mov_b32 s3, 0x19200
	v_add3_u32 v18, v18, v19, s3
	ds_read_b128 v[18:21], v18
	v_mov_b32_e32 v26, 4
	v_lshlrev_b32_sdwa v26, v26, v0 dst_sel:DWORD dst_unused:UNUSED_PAD src0_sel:DWORD src1_sel:BYTE_0
	v_mov_b32_e32 v27, 0
	v_lshl_add_u64 v[24:25], v[24:25], 0, v[26:27]
	s_waitcnt lgkmcnt(0)
	global_store_dwordx4 v[24:25], v[18:21], off sc1

.LBB0_34:
	s_and_b64 vcc, exec, s[8:9]
	s_cbranch_vccz .LBB0_40
	v_cmp_eq_u32_e32 vcc, 0, v0
	s_and_saveexec_b64 s[6:7], vcc
	s_cbranch_execz .LBB0_37
	v_mov_b32_e32 v18, 0x1d800
	v_mov_b32_e32 v20, 0x1d840
	ds_read_b64 v[18:19], v18
	ds_read_b64 v[20:21], v20
	v_mov_b32_e32 v24, 0x1d880
	v_mov_b32_e32 v26, 0x1d8c0
	ds_read_b64 v[24:25], v24
	ds_read_b64 v[26:27], v26
	s_waitcnt lgkmcnt(0)
	v_max_f32_e32 v18, v18, v18
	v_max_f32_e32 v20, v20, v20
	v_max_f32_e32 v18, v18, v20
	v_add_f32_e32 v19, v19, v21
	v_add_f32_e32 v19, v19, v25
	v_max3_f32 v21, v18, v24, v26
	v_mov_b32_e32 v18, 0x1d900
	v_add_f32_e32 v30, v19, v27
	v_mov_b32_e32 v19, 0x1d940
	v_mov_b32_e32 v20, 0x1d980
	ds_read_b64 v[24:25], v18
	ds_read_b64 v[26:27], v19
	ds_read_b64 v[28:29], v20
	v_mov_b32_e32 v18, 0x1d9c0
	ds_read_b96 v[18:20], v18
	s_mov_b32 s10, 0x3b800000
	s_waitcnt lgkmcnt(2)
	v_max3_f32 v21, v21, v24, v26
	s_waitcnt lgkmcnt(0)
	v_add_f32_e32 v20, v30, v25
	s_mov_b32 s11, 0x3eaab368
	v_max3_f32 v24, v21, v28, v18
	v_mul_f32_e32 v25, v24, v24
	v_add_f32_e32 v20, v20, v27
	v_pk_mul_f32 v[26:27], v[24:25], s[10:11]
	v_add_f32_e32 v20, v20, v29
	v_mov_b32_e32 v28, v26
	v_mul_f32_e32 v21, 0x3ec51eb8, v25
	v_mov_b32_e32 v18, v19
	v_mov_b32_e32 v19, v26
	v_fmac_f32_e32 v28, v24, v27
	v_pk_add_f32 v[18:19], v[20:21], v[18:19]
	s_mov_b32 s3, 0x3a83126f
	v_mul_f32_e32 v20, v18, v28
	s_mov_b64 s[8:9], s[70:71]
	v_cmp_nge_f32_e32 vcc, s3, v20
	v_mul_f32_e32 v18, v18, v19
	s_and_b64 s[10:11], vcc, exec
	v_cmp_nge_f32_e32 vcc, s3, v18
	s_cselect_b32 s12, 3, 2
	s_and_b64 s[10:11], vcc, exec
	s_cselect_b32 s12, s12, 1
	s_ashr_i32 s3, s2, 31
	s_lshl_b64 s[10:11], s[2:3], 2
	s_waitcnt lgkmcnt(0)
	s_add_u32 s8, s8, s10
	s_addc_u32 s9, s9, s11
	v_mov_b32_e32 v18, 0
	v_mov_b32_e32 v19, s12
	global_store_dword v18, v19, s[8:9] sc1
.LBB0_37:
	s_or_b64 exec, exec, s[6:7]
	s_movk_i32 s3, 0x200
	v_cmp_gt_u32_e32 vcc, s3, v0
	s_and_saveexec_b64 s[6:7], vcc
	s_cbranch_execz .LBB0_39
	v_lshrrev_b32_e32 v18, 4, v0
	v_bfe_u32 v18, v18, 3, 1
	s_mov_b64 s[0:1], s[60:61]
	v_lshl_or_b32 v18, s2, 1, v18
	v_lshrrev_b32_e32 v21, 8, v0
	v_ashrrev_i32_e32 v19, 31, v18
	v_lshlrev_b32_e32 v24, 10, v21
	v_mov_b32_e32 v25, 0
	v_lshl_add_u64 v[18:19], v[18:19], 2, v[24:25]
	v_lshrrev_b32_e32 v24, 2, v1
	v_or_b32_e32 v18, v18, v24
	v_bfe_u32 v20, v0, 4, 4
	v_lshlrev_b64 v[18:19], 9, v[18:19]
	s_waitcnt lgkmcnt(0)
	v_lshl_add_u64 v[26:27], s[0:1], 0, v[18:19]
	v_mul_u32_u24_e32 v18, 0x110, v20
	s_movk_i32 s0, 0x1100
	v_mad_u32_u24 v18, v21, s0, v18
	v_lshlrev_b32_e32 v1, 4, v1
	s_mov_b32 s0, 0x19200
	v_add3_u32 v1, v18, v1, s0
	ds_read_b128 v[18:21], v1
	v_lshlrev_b32_e32 v24, 7, v0
	v_and_b32_e32 v24, 0x180, v24
	v_lshl_add_u64 v[26:27], v[26:27], 0, v[24:25]
	v_and_b32_e32 v24, 0x70, v0
	v_lshl_add_u64 v[0:1], v[26:27], 0, v[24:25]
	s_waitcnt lgkmcnt(0)
	global_store_dwordx4 v[0:1], v[18:21], off sc1
